# retln row loop: the row's 8 data loads issued together with its stats load (one load round trip per row instead of five); on top of stack4
# baseline (speedup 1.0000x reference)
; __device__ __forceinline__ unsigned cvtpk(float lo, float hi) { f32x2_t v = {lo, hi}; bf16x2_t b = __builtin_convertvector(v, bf16x2_t); return __builtin_bit_cast(unsigned, b); }
; __device__ __forceinline__ float bflo(unsigned u) { return __uint_as_float(u << 16); }
; __device__ __forceinline__ float bfhi(unsigned u) { return __uint_as_float(u & 0xffff0000u); }
; __device__ __forceinline__ void phase_retln(const bf16* Opre, const float* stats, const bf16* Gi, bf16* Gt, const float* gn, int gw, int NGW, int lane) {
;     ...
;     for (int m = gw; m < M; m += NGW) {
;         f32x2v st = *(const f32x2v*)(stats + ((size_t)m * 64 + lane) * 2);
;         float s = st.x, q = st.y;
;         s += __shfl_xor(s, 1); q += __shfl_xor(q, 1); s += __shfl_xor(s, 2); q += __shfl_xor(q, 2); s += __shfl_xor(s, 4); q += __shfl_xor(q, 4);
;         const float mean_l = s * (1.0f / 256.0f), var_l = q * (1.0f / 256.0f) - mean_l * mean_l, rstd_l = 1.0f / sqrtf(fmaxf(var_l, 0.f) + EPS);
;         const v4u* op = (const v4u*)(Opre + (size_t)m * LDT) + lane; v4u* gp = (v4u*)(Gt + (size_t)m * LDT) + lane; const v4u* gi = (const v4u*)(Gi + (size_t)m * LDT) + lane;
; #pragma unroll
;         for (int j = 0; j < 4; ++j) { const float mean = __shfl(mean_l, 8 * (2 * j + hs)), rstd = __shfl(rstd_l, 8 * (2 * j + hs));
;             const v4u ow = op[64 * j], gw2 = gi[64 * j];
;             v4u y; y.x = cvtpk((bflo(ow.x) - mean) * rstd * ga[j][0] * bflo(gw2.x), (bfhi(ow.x) - mean) * rstd * ga[j][1] * bfhi(gw2.x));
;             y.y = cvtpk((bflo(ow.y) - mean) * rstd * ga[j][2] * bflo(gw2.y), (bfhi(ow.y) - mean) * rstd * ga[j][3] * bfhi(gw2.y));
;             y.z = cvtpk((bflo(ow.z) - mean) * rstd * gb[j][0] * bflo(gw2.z), (bfhi(ow.z) - mean) * rstd * gb[j][1] * bfhi(gw2.z));
;             y.w = cvtpk((bflo(ow.w) - mean) * rstd * gb[j][2] * bflo(gw2.w), (bfhi(ow.w) - mean) * rstd * gb[j][3] * bfhi(gw2.w));
;             gp[64 * j] = y; }
.LBB0_524:
	v_lshl_add_u64 v[40:41], s[4:5], 0, v[38:39]
	global_load_dwordx2 v[40:41], v[40:41], off
	v_lshl_add_u64 v[100:101], s[4:5], 0, v[36:37]
	v_add_co_u32_e32 v102, vcc, 0x61c00000, v100
	v_addc_co_u32_e32 v103, vcc, 0, v101, vcc
	v_add_co_u32_e32 v104, vcc, 0x31400000, v100
	v_addc_co_u32_e32 v105, vcc, 0, v101, vcc
	global_load_dwordx4 v[68:71], v[102:103], off
	global_load_dwordx4 v[72:75], v[104:105], off
	global_load_dwordx4 v[76:79], v[102:103], off offset:1024
	global_load_dwordx4 v[80:83], v[104:105], off offset:1024
	global_load_dwordx4 v[84:87], v[102:103], off offset:2048
	global_load_dwordx4 v[88:91], v[104:105], off offset:2048
	global_load_dwordx4 v[92:95], v[102:103], off offset:3072
	global_load_dwordx4 v[96:99], v[104:105], off offset:3072
	s_mov_b32 s2, 0x3b800000
	s_add_i32 s0, s0, s76
	v_lshl_add_u64 v[38:39], v[38:39], 0, s[10:11]
	s_cmp_lt_i32 s0, 0x8000
	s_waitcnt vmcnt(8)
	ds_bpermute_b32 v48, v3, v40
	ds_bpermute_b32 v49, v3, v41
	s_waitcnt lgkmcnt(0)
	v_pk_add_f32 v[40:41], v[40:41], v[48:49]
	ds_bpermute_b32 v48, v42, v40
	ds_bpermute_b32 v49, v42, v41
	s_waitcnt lgkmcnt(0)
	v_pk_add_f32 v[40:41], v[40:41], v[48:49]
	ds_bpermute_b32 v48, v43, v40
	ds_bpermute_b32 v49, v43, v41
	s_waitcnt lgkmcnt(0)
	v_pk_add_f32 v[40:41], v[40:41], v[48:49]
	s_nop 0
	v_pk_mul_f32 v[40:41], v[40:41], s[2:3] op_sel_hi:[1,0]
	ds_bpermute_b32 v56, v44, v40
	v_fma_f32 v41, -v40, v40, v41
	v_max_f32_e32 v41, 0, v41
	v_add_f32_e32 v41, 0x358637bd, v41
	v_cmp_gt_f32_e32 vcc, s8, v41
	v_mul_f32_e32 v48, 0x4f800000, v41
	s_nop 0
	v_cndmask_b32_e32 v41, v41, v48, vcc
	v_sqrt_f32_e32 v48, v41
	s_nop 0
	v_add_u32_e32 v49, -1, v48
	v_fma_f32 v50, -v49, v48, v41
	v_cmp_ge_f32_e64 s[6:7], 0, v50
	v_add_u32_e32 v50, 1, v48
	s_nop 0
	v_cndmask_b32_e64 v49, v48, v49, s[6:7]
	v_fma_f32 v48, -v50, v48, v41
	v_cmp_lt_f32_e64 s[6:7], 0, v48
	s_nop 1
	v_cndmask_b32_e64 v48, v49, v50, s[6:7]
	v_mul_f32_e32 v49, 0x37800000, v48
	v_cndmask_b32_e32 v48, v48, v49, vcc
	v_cmp_class_f32_e32 vcc, v41, v211
	s_nop 1
	v_cndmask_b32_e32 v41, v48, v41, vcc
	v_div_scale_f32 v48, s[2:3], v41, v41, 1.0
	v_rcp_f32_e32 v49, v48
	s_mov_b32 s2, 0x61c00000
	v_fma_f32 v50, -v48, v49, 1.0
	v_fmac_f32_e32 v49, v50, v49
	v_div_scale_f32 v50, vcc, 1.0, v41, 1.0
	v_mul_f32_e32 v51, v50, v49
	v_fma_f32 v52, -v48, v51, v50
	v_fmac_f32_e32 v51, v52, v49
	v_fma_f32 v48, -v48, v51, v50
	v_lshl_add_u64 v[52:53], s[4:5], 0, v[36:37]
	v_div_fmas_f32 v48, v48, v49, v51
	v_add_co_u32_e32 v60, vcc, s2, v52
	v_div_fixup_f32 v41, v48, v41, 1.0
	s_nop 0
	v_addc_co_u32_e32 v61, vcc, 0, v53, vcc
	s_mov_b32 s2, 0x31400000
	v_add_co_u32_e32 v62, vcc, s2, v52
	ds_bpermute_b32 v58, v44, v41
	s_nop 0
	v_addc_co_u32_e32 v63, vcc, 0, v53, vcc
	v_lshl_add_u64 v[36:37], v[36:37], 0, s[88:89]
	s_waitcnt vmcnt(0)
	v_lshlrev_b32_e32 v64, 16, v68
	v_and_b32_e32 v65, 0xffff0000, v68
	s_waitcnt lgkmcnt(1)
	v_pk_add_f32 v[64:65], v[64:65], v[56:57] op_sel_hi:[1,0] neg_lo:[0,1] neg_hi:[0,1]
	v_lshlrev_b32_e32 v66, 16, v72
	s_waitcnt lgkmcnt(0)
	v_pk_mul_f32 v[64:65], v[64:65], v[58:59] op_sel_hi:[1,0]
	v_and_b32_e32 v67, 0xffff0000, v72
	v_pk_mul_f32 v[64:65], v[28:29], v[64:65]
	v_lshlrev_b32_e32 v52, 16, v73
	v_pk_mul_f32 v[64:65], v[64:65], v[66:67]
	v_and_b32_e32 v53, 0xffff0000, v73
	v_cvt_pk_bf16_f32 v48, v64, v65
	v_lshlrev_b32_e32 v64, 16, v69
	v_and_b32_e32 v65, 0xffff0000, v69
	v_pk_add_f32 v[64:65], v[64:65], v[56:57] op_sel_hi:[1,0] neg_lo:[0,1] neg_hi:[0,1]
	s_nop 0
	v_pk_mul_f32 v[64:65], v[64:65], v[58:59] op_sel_hi:[1,0]
	s_nop 0
	v_pk_mul_f32 v[64:65], v[30:31], v[64:65]
	s_nop 0
	v_pk_mul_f32 v[52:53], v[64:65], v[52:53]
	v_lshlrev_b32_e32 v64, 16, v74
	v_cvt_pk_bf16_f32 v49, v52, v53
	v_lshlrev_b32_e32 v52, 16, v70
	v_and_b32_e32 v53, 0xffff0000, v70
	v_pk_add_f32 v[52:53], v[52:53], v[56:57] op_sel_hi:[1,0] neg_lo:[0,1] neg_hi:[0,1]
	v_and_b32_e32 v65, 0xffff0000, v74
	v_pk_mul_f32 v[52:53], v[52:53], v[58:59] op_sel_hi:[1,0]
	v_lshlrev_b32_e32 v54, 16, v75
	v_pk_mul_f32 v[52:53], v[32:33], v[52:53]
	v_and_b32_e32 v55, 0xffff0000, v75
	v_pk_mul_f32 v[52:53], v[52:53], v[64:65]
	s_nop 0
	v_cvt_pk_bf16_f32 v50, v52, v53
	v_lshlrev_b32_e32 v52, 16, v71
	v_and_b32_e32 v53, 0xffff0000, v71
	v_pk_add_f32 v[52:53], v[52:53], v[56:57] op_sel_hi:[1,0] neg_lo:[0,1] neg_hi:[0,1]
	ds_bpermute_b32 v56, v45, v40
	v_pk_mul_f32 v[52:53], v[52:53], v[58:59] op_sel_hi:[1,0]
	ds_bpermute_b32 v58, v45, v41
	v_pk_mul_f32 v[52:53], v[34:35], v[52:53]
	s_nop 0
	v_pk_mul_f32 v[52:53], v[52:53], v[54:55]
	s_nop 0
	v_cvt_pk_bf16_f32 v51, v52, v53
	global_store_dwordx4 v[62:63], v[48:51], off
	s_nop 0
	v_lshlrev_b32_e32 v64, 16, v76
	v_and_b32_e32 v65, 0xffff0000, v76
	s_waitcnt lgkmcnt(1)
	v_pk_add_f32 v[64:65], v[64:65], v[56:57] op_sel_hi:[1,0] neg_lo:[0,1] neg_hi:[0,1]
	v_lshlrev_b32_e32 v66, 16, v80
	s_waitcnt lgkmcnt(0)
; __device__ __forceinline__ unsigned cvtpk(float lo, float hi) { f32x2_t v = {lo, hi}; bf16x2_t b = __builtin_convertvector(v, bf16x2_t); return __builtin_bit_cast(unsigned, b); }
; __device__ __forceinline__ float bflo(unsigned u) { return __uint_as_float(u << 16); }
; __device__ __forceinline__ float bfhi(unsigned u) { return __uint_as_float(u & 0xffff0000u); }
; __device__ __forceinline__ void phase_retln(const bf16* Opre, const float* stats, const bf16* Gi, bf16* Gt, const float* gn, int gw, int NGW, int lane) {
;     ...
;         const v4u* op = (const v4u*)(Opre + (size_t)m * LDT) + lane; v4u* gp = (v4u*)(Gt + (size_t)m * LDT) + lane; const v4u* gi = (const v4u*)(Gi + (size_t)m * LDT) + lane;
; #pragma unroll
;         for (int j = 0; j < 4; ++j) { const float mean = __shfl(mean_l, 8 * (2 * j + hs)), rstd = __shfl(rstd_l, 8 * (2 * j + hs));
;             const v4u ow = op[64 * j], gw2 = gi[64 * j];
;             v4u y; y.x = cvtpk((bflo(ow.x) - mean) * rstd * ga[j][0] * bflo(gw2.x), (bfhi(ow.x) - mean) * rstd * ga[j][1] * bfhi(gw2.x));
;             y.y = cvtpk((bflo(ow.y) - mean) * rstd * ga[j][2] * bflo(gw2.y), (bfhi(ow.y) - mean) * rstd * ga[j][3] * bfhi(gw2.y));
;             y.z = cvtpk((bflo(ow.z) - mean) * rstd * gb[j][0] * bflo(gw2.z), (bfhi(ow.z) - mean) * rstd * gb[j][1] * bfhi(gw2.z));
;             y.w = cvtpk((bflo(ow.w) - mean) * rstd * gb[j][2] * bflo(gw2.w), (bfhi(ow.w) - mean) * rstd * gb[j][3] * bfhi(gw2.w));
;             gp[64 * j] = y; }
	v_pk_mul_f32 v[64:65], v[64:65], v[58:59] op_sel_hi:[1,0]
	v_and_b32_e32 v67, 0xffff0000, v80
	v_pk_mul_f32 v[64:65], v[20:21], v[64:65]
	v_lshlrev_b32_e32 v52, 16, v81
	v_pk_mul_f32 v[64:65], v[64:65], v[66:67]
	v_and_b32_e32 v53, 0xffff0000, v81
	v_cvt_pk_bf16_f32 v48, v64, v65
	v_lshlrev_b32_e32 v64, 16, v77
	v_and_b32_e32 v65, 0xffff0000, v77
	v_pk_add_f32 v[64:65], v[64:65], v[56:57] op_sel_hi:[1,0] neg_lo:[0,1] neg_hi:[0,1]
	s_nop 0
	v_pk_mul_f32 v[64:65], v[64:65], v[58:59] op_sel_hi:[1,0]
	s_nop 0
	v_pk_mul_f32 v[64:65], v[22:23], v[64:65]
	s_nop 0
	v_pk_mul_f32 v[52:53], v[64:65], v[52:53]
	v_lshlrev_b32_e32 v64, 16, v82
	v_cvt_pk_bf16_f32 v49, v52, v53
	v_lshlrev_b32_e32 v52, 16, v78
	v_and_b32_e32 v53, 0xffff0000, v78
	v_pk_add_f32 v[52:53], v[52:53], v[56:57] op_sel_hi:[1,0] neg_lo:[0,1] neg_hi:[0,1]
	v_and_b32_e32 v65, 0xffff0000, v82
	v_pk_mul_f32 v[52:53], v[52:53], v[58:59] op_sel_hi:[1,0]
	v_lshlrev_b32_e32 v54, 16, v83
	v_pk_mul_f32 v[52:53], v[24:25], v[52:53]
	v_and_b32_e32 v55, 0xffff0000, v83
	v_pk_mul_f32 v[52:53], v[52:53], v[64:65]
	s_nop 0
	v_cvt_pk_bf16_f32 v50, v52, v53
	v_lshlrev_b32_e32 v52, 16, v79
	v_and_b32_e32 v53, 0xffff0000, v79
	v_pk_add_f32 v[52:53], v[52:53], v[56:57] op_sel_hi:[1,0] neg_lo:[0,1] neg_hi:[0,1]
	ds_bpermute_b32 v56, v46, v40
	v_pk_mul_f32 v[52:53], v[52:53], v[58:59] op_sel_hi:[1,0]
	ds_bpermute_b32 v58, v46, v41
	v_pk_mul_f32 v[52:53], v[26:27], v[52:53]
	ds_bpermute_b32 v40, v47, v40
	v_pk_mul_f32 v[52:53], v[52:53], v[54:55]
	s_nop 0
	v_cvt_pk_bf16_f32 v51, v52, v53
	global_store_dwordx4 v[62:63], v[48:51], off offset:1024
	s_nop 0
	v_lshlrev_b32_e32 v64, 16, v84
	v_and_b32_e32 v65, 0xffff0000, v84
	s_waitcnt lgkmcnt(2)
	v_pk_add_f32 v[64:65], v[64:65], v[56:57] op_sel_hi:[1,0] neg_lo:[0,1] neg_hi:[0,1]
	v_lshlrev_b32_e32 v66, 16, v88
	s_waitcnt lgkmcnt(1)
	v_pk_mul_f32 v[64:65], v[64:65], v[58:59] op_sel_hi:[1,0]
	v_and_b32_e32 v67, 0xffff0000, v88
	v_pk_mul_f32 v[64:65], v[12:13], v[64:65]
	v_lshlrev_b32_e32 v52, 16, v89
	v_pk_mul_f32 v[64:65], v[64:65], v[66:67]
	v_and_b32_e32 v53, 0xffff0000, v89
	v_cvt_pk_bf16_f32 v48, v64, v65
	v_lshlrev_b32_e32 v64, 16, v85
	v_and_b32_e32 v65, 0xffff0000, v85
	v_pk_add_f32 v[64:65], v[64:65], v[56:57] op_sel_hi:[1,0] neg_lo:[0,1] neg_hi:[0,1]
	s_nop 0
	v_pk_mul_f32 v[64:65], v[64:65], v[58:59] op_sel_hi:[1,0]
	s_nop 0
	v_pk_mul_f32 v[64:65], v[14:15], v[64:65]
	s_nop 0
	v_pk_mul_f32 v[52:53], v[64:65], v[52:53]
	v_lshlrev_b32_e32 v64, 16, v90
	v_cvt_pk_bf16_f32 v49, v52, v53
	v_lshlrev_b32_e32 v52, 16, v86
	v_and_b32_e32 v53, 0xffff0000, v86
	v_pk_add_f32 v[52:53], v[52:53], v[56:57] op_sel_hi:[1,0] neg_lo:[0,1] neg_hi:[0,1]
	v_and_b32_e32 v65, 0xffff0000, v90
	v_pk_mul_f32 v[52:53], v[52:53], v[58:59] op_sel_hi:[1,0]
	v_lshlrev_b32_e32 v54, 16, v91
	v_pk_mul_f32 v[52:53], v[16:17], v[52:53]
	v_and_b32_e32 v55, 0xffff0000, v91
	v_pk_mul_f32 v[52:53], v[52:53], v[64:65]
	s_nop 0
	v_cvt_pk_bf16_f32 v50, v52, v53
	v_lshlrev_b32_e32 v52, 16, v87
	v_and_b32_e32 v53, 0xffff0000, v87
	v_pk_add_f32 v[52:53], v[52:53], v[56:57] op_sel_hi:[1,0] neg_lo:[0,1] neg_hi:[0,1]
	ds_bpermute_b32 v56, v47, v41
	v_pk_mul_f32 v[52:53], v[52:53], v[58:59] op_sel_hi:[1,0]
	s_nop 0
	v_pk_mul_f32 v[52:53], v[18:19], v[52:53]
	s_nop 0
	v_pk_mul_f32 v[52:53], v[52:53], v[54:55]
	s_nop 0
	v_cvt_pk_bf16_f32 v51, v52, v53
	global_store_dwordx4 v[62:63], v[48:51], off offset:2048
	s_nop 0
	v_lshlrev_b32_e32 v58, 16, v92
	v_and_b32_e32 v59, 0xffff0000, v92
	s_waitcnt lgkmcnt(1)
	v_pk_add_f32 v[58:59], v[58:59], v[40:41] op_sel_hi:[1,0] neg_lo:[0,1] neg_hi:[0,1]
	v_lshlrev_b32_e32 v60, 16, v96
	s_waitcnt lgkmcnt(0)
	v_pk_mul_f32 v[58:59], v[58:59], v[56:57] op_sel_hi:[1,0]
	v_and_b32_e32 v61, 0xffff0000, v96
	v_pk_mul_f32 v[58:59], v[4:5], v[58:59]
	v_lshlrev_b32_e32 v52, 16, v97
	v_pk_mul_f32 v[58:59], v[58:59], v[60:61]
	v_and_b32_e32 v53, 0xffff0000, v97
	v_cvt_pk_bf16_f32 v48, v58, v59
	v_lshlrev_b32_e32 v58, 16, v93
	v_and_b32_e32 v59, 0xffff0000, v93
	v_pk_add_f32 v[58:59], v[58:59], v[40:41] op_sel_hi:[1,0] neg_lo:[0,1] neg_hi:[0,1]
	s_nop 0
	v_pk_mul_f32 v[58:59], v[58:59], v[56:57] op_sel_hi:[1,0]
	s_nop 0
	v_pk_mul_f32 v[58:59], v[6:7], v[58:59]
	s_nop 0
	v_pk_mul_f32 v[52:53], v[58:59], v[52:53]
	v_lshlrev_b32_e32 v58, 16, v98
	v_cvt_pk_bf16_f32 v49, v52, v53
	v_lshlrev_b32_e32 v52, 16, v94
	v_and_b32_e32 v53, 0xffff0000, v94
	v_pk_add_f32 v[52:53], v[52:53], v[40:41] op_sel_hi:[1,0] neg_lo:[0,1] neg_hi:[0,1]
	v_and_b32_e32 v59, 0xffff0000, v98
	v_pk_mul_f32 v[52:53], v[52:53], v[56:57] op_sel_hi:[1,0]
	s_nop 0
	v_pk_mul_f32 v[52:53], v[8:9], v[52:53]
	s_nop 0
	v_pk_mul_f32 v[52:53], v[52:53], v[58:59]
	s_nop 0
	v_cvt_pk_bf16_f32 v50, v52, v53
	v_lshlrev_b32_e32 v52, 16, v95
	v_and_b32_e32 v53, 0xffff0000, v95
	v_pk_add_f32 v[40:41], v[52:53], v[40:41] op_sel_hi:[1,0] neg_lo:[0,1] neg_hi:[0,1]
	v_lshlrev_b32_e32 v52, 16, v99
	v_pk_mul_f32 v[40:41], v[40:41], v[56:57] op_sel_hi:[1,0]
	v_and_b32_e32 v53, 0xffff0000, v99
	v_pk_mul_f32 v[40:41], v[10:11], v[40:41]
	s_nop 0
	v_pk_mul_f32 v[40:41], v[40:41], v[52:53]
	s_nop 0
	v_cvt_pk_bf16_f32 v51, v40, v41
	global_store_dwordx4 v[62:63], v[48:51], off offset:3072
	s_cbranch_scc1 .LBB0_524
